# passCU: Sel one-hot operand fetched from a 16-entry LDS lookup table indexed by 4 mask bits (replaces 32 VALU per tile)
# speedup vs baseline: 1.0246x; 1.0105x over previous
.LBB7_8:
	s_load_dwordx2 s[12:13], s[0:1], 0x68
	s_lshl_b32 s17, s6, 5
	s_lshl_b32 s18, s10, 5
	s_sub_i32 s4, s18, s17
	s_ashr_i32 s16, s4, 5
	s_cmp_lt_i32 s16, 1
	v_and_b32_e32 v1, 63, v0
	s_cbranch_scc1 .LBB7_13
	s_load_dwordx8 s[4:11], s[0:1], 0x0
	s_load_dwordx2 s[14:15], s[0:1], 0x20
	v_and_b32_e32 v54, 7, v1
	v_lshlrev_b32_e32 v54, 4, v54
	v_lshrrev_b32_e32 v56, 3, v1
	v_lshlrev_b32_e32 v55, 1, v54
	ds_read_b128 v[2:5], v55 offset:18432
	ds_read_b128 v[6:9], v55 offset:18448
	ds_read_b128 v[10:13], v55 offset:18944
	ds_read_b128 v[14:17], v55 offset:18960
	ds_read_b128 v[18:21], v55 offset:18688
	ds_read_b128 v[22:25], v55 offset:18704
	s_mul_i32 s21, s3, 0x1200
	s_add_i32 s21, s21, 0x4b00
	v_mul_u32_u24_e32 v58, 0x240, v56
	v_add3_u32 v58, v58, v54, s21
	v_and_b32_e32 v59, 31, v1
	v_mul_u32_u24_e32 v59, 0x90, v59
	v_lshrrev_b32_e32 v57, 5, v1
	v_lshlrev_b32_e32 v57, 6, v57
	v_add3_u32 v59, v59, v57, s21
	v_lshlrev_b32_e32 v56, 4, v56
	v_lshlrev_b32_e32 v57, 4, v1
	v_mov_b32_e32 v50, 0
	v_mov_b32_e32 v51, 0
	v_mov_b32_e32 v52, 0
	v_mov_b32_e32 v53, 0
	s_lshl_b32 s20, s17, 2
	s_add_i32 s20, s20, 0x100
	s_mov_b32 s22, 0x3d0880
	s_mov_b32 s52, 0xffff0000
	s_waitcnt vmcnt(0) lgkmcnt(0)
	v_mov_b32_e32 v26, v104
	v_mov_b32_e32 v27, v105
	v_mov_b32_e32 v28, v106
	v_mov_b32_e32 v29, v107
	v_mov_b32_e32 v30, v108
	v_mov_b32_e32 v31, v109
	v_mov_b32_e32 v32, v110
	v_mov_b32_e32 v33, v111
	v_mov_b32_e32 v38, v112
	v_mov_b32_e32 v39, v113
	v_mov_b32_e32 v40, v114
	v_mov_b32_e32 v41, v115
	v_mov_b32_e32 v34, v100
	v_mov_b32_e32 v35, v101
	v_mov_b32_e32 v36, v102
	v_mov_b32_e32 v37, v103

.LBB8_4:
	s_load_dwordx2 s[12:13], s[0:1], 0xa8
	s_load_dwordx2 s[18:19], s[0:1], 0x98
	s_waitcnt lgkmcnt(0)
	s_sub_i32 s4, s28, s20
	s_add_i32 s4, s4, 31
	v_and_b32_e32 v1, 63, v0
	s_ashr_i32 s15, s4, 5
	s_cmp_lt_i32 s15, 1
	v_add_u32_e32 v90, s14, v98
	v_and_b32_e32 v100, 32, v0
	v_lshlrev_b32_e32 v99, 4, v1
	s_cbranch_scc1 .LBB8_7
	s_load_dwordx8 s[4:11], s[0:1], 0x0
	s_load_dwordx2 s[24:25], s[0:1], 0x20
	s_load_dwordx2 s[30:31], s[0:1], 0x80
	s_load_dwordx2 s[48:49], s[0:1], 0x90
	v_and_b32_e32 v34, 7, v1
	v_lshlrev_b32_e32 v34, 4, v34
	v_lshrrev_b32_e32 v35, 3, v1
	s_lshl_b32 s32, s3, 12
	s_add_i32 s33, s32, 0x2000
	s_add_i32 s32, s32, 0xb500
	s_cmp_lt_u32 s3, 2
	s_cselect_b32 s32, s33, s32
	v_lshlrev_b32_e32 v36, 1, v35
	v_and_b32_e32 v36, 7, v36
	v_or_b32_e32 v37, 1, v36
	v_lshlrev_b32_e32 v36, 4, v36
	v_lshlrev_b32_e32 v37, 4, v37
	v_xor_b32_e32 v36, v36, v34
	v_xor_b32_e32 v37, v37, v34
	v_lshl_add_u32 v39, v35, 9, s32
	v_add_u32_e32 v36, v36, v39
	v_add_u32_e32 v37, v37, v39
	v_lshrrev_b32_e32 v38, 1, v98
	v_and_b32_e32 v38, 7, v38
	v_lshrrev_b32_e32 v39, 3, v100
	v_xor_b32_e32 v38, v38, v39
	v_lshlrev_b32_e32 v38, 4, v38
	v_lshl_add_u32 v39, v98, 7, s32
	v_add_u32_e32 v38, v38, v39
	v_lshlrev_b32_e32 v35, 4, v35
	s_mov_b32 s35, 0x1869f
	s_mov_b32 s65, 0xffff0000
	v_mov_b32_e32 v2, 0
	v_mov_b32_e32 v3, 0
	v_mov_b32_e32 v4, 0
	v_mov_b32_e32 v5, 0
	v_mov_b32_e32 v6, 0
	v_mov_b32_e32 v7, 0
	v_mov_b32_e32 v8, 0
	v_mov_b32_e32 v9, 0
	v_mov_b32_e32 v10, 0
	v_mov_b32_e32 v11, 0
	v_mov_b32_e32 v12, 0
	v_mov_b32_e32 v13, 0
	v_mov_b32_e32 v14, 0
	v_mov_b32_e32 v15, 0
	v_mov_b32_e32 v16, 0
	v_mov_b32_e32 v17, 0
	v_mov_b32_e32 v18, 0
	v_mov_b32_e32 v19, 0
	v_mov_b32_e32 v20, 0
	v_mov_b32_e32 v21, 0
	v_mov_b32_e32 v22, 0
	v_mov_b32_e32 v23, 0
	v_mov_b32_e32 v24, 0
	v_mov_b32_e32 v25, 0
	v_mov_b32_e32 v26, 0
	v_mov_b32_e32 v27, 0
	v_mov_b32_e32 v28, 0
	v_mov_b32_e32 v29, 0
	v_mov_b32_e32 v30, 0
	v_mov_b32_e32 v31, 0
	v_mov_b32_e32 v32, 0
	v_mov_b32_e32 v33, 0
	s_waitcnt vmcnt(0) lgkmcnt(0)
	v_mov_b32_e32 v42, v70
	v_mov_b32_e32 v43, v71
	v_mov_b32_e32 v44, v72
	v_mov_b32_e32 v45, v73
	v_mov_b32_e32 v46, v74
	v_mov_b32_e32 v47, v75
	v_mov_b32_e32 v48, v76
	v_mov_b32_e32 v49, v77
	v_mov_b32_e32 v50, v78
	v_mov_b32_e32 v51, v79
	v_mov_b32_e32 v52, v80
	v_mov_b32_e32 v53, v81
	v_lshlrev_b32_e32 v39, 2, v90
	global_load_dword v40, v39, s[30:31]
	global_load_dword v41, v39, s[30:31] offset:4
	s_lshl_b32 s34, s20, 2
	v_min_u32_e32 v42, s35, v42
	v_min_u32_e32 v46, s35, v46
	v_min_u32_e32 v43, s35, v43
	v_min_u32_e32 v47, s35, v47
	v_min_u32_e32 v44, s35, v44
	v_min_u32_e32 v48, s35, v48
	v_min_u32_e32 v45, s35, v45
	v_min_u32_e32 v49, s35, v49
	v_lshl_or_b32 v42, v42, 7, v34
	v_lshl_or_b32 v46, v46, 7, v34
	v_lshl_or_b32 v43, v43, 7, v34
	v_lshl_or_b32 v47, v47, 7, v34
	v_lshl_or_b32 v44, v44, 7, v34
	v_lshl_or_b32 v48, v48, 7, v34
	v_lshl_or_b32 v45, v45, 7, v34
	v_lshl_or_b32 v49, v49, 7, v34
	global_load_dwordx4 v[70:73], v42, s[24:25]
	global_load_dwordx4 v[74:77], v43, s[24:25]
	global_load_dwordx4 v[78:81], v44, s[24:25]
	global_load_dwordx4 v[82:85], v45, s[24:25]
	global_load_dwordx4 v[86:89], v46, s[10:11]
	global_load_dwordx4 v[90:93], v47, s[10:11]
	global_load_dwordx4 v[94:97], v48, s[10:11]
	global_load_dwordx4 v[102:105], v49, s[10:11]
	s_add_i32 s34, s34, 0x80
	v_add_u32_e32 v39, s34, v35
	global_load_dwordx4 v[42:45], v39, s[4:5]
	global_load_dwordx4 v[46:49], v39, s[6:7]
	s_cmp_lt_u32 s3, 4
	s_cbranch_scc1 .Lcu_nopri
	s_setprio 1
.Lcu_nopri:
	s_mov_b32 s66, 0x13500
	v_and_b32_e32 v101, 15, v1
	v_bfe_u32 v110, v101, 0, 2
	v_lshl_or_b32 v110, v110, 15, v110
	v_and_b32_e32 v110, 0x10001, v110
	v_mul_u32_u24_e32 v110, 0x3f80, v110
	v_bfe_u32 v111, v101, 2, 2
	v_lshl_or_b32 v111, v111, 15, v111
	v_and_b32_e32 v111, 0x10001, v111
	v_mul_u32_u24_e32 v111, 0x3f80, v111
	v_lshl_add_u32 v39, v101, 3, s66
	ds_write_b64 v39, v[110:111]
	v_lshlrev_b32_e32 v39, 1, v34
	ds_read_b128 v[112:115], v39 offset:53248
	ds_read_b128 v[116:119], v39 offset:53760
	ds_read_b128 v[120:123], v39 offset:53504

.Lcu_skip1:
	v_subrev_u32_e32 v101, s20, v40
	v_subrev_u32_e32 v110, s20, v41
	v_med3_i32 v101, v101, 0, 32
	v_med3_i32 v110, v110, 0, 32
	v_lshlrev_b64 v[54:55], v101, 1
	v_lshlrev_b64 v[56:57], v110, 1
	v_add_u32_e32 v54, -1, v54
	v_add_u32_e32 v56, -1, v56
	v_xor_b32_e32 v101, v54, v56
	v_lshrrev_b32_e32 v110, 3, v100
	v_lshrrev_b32_e32 v101, v110, v101
	v_bfe_u32 v110, v101, 0, 4
	v_lshl_add_u32 v110, v110, 3, s66
	ds_read_b64 v[54:55], v110
	v_bfe_u32 v111, v101, 8, 4
	v_lshl_add_u32 v111, v111, 3, s66
	ds_read_b64 v[56:57], v111
	v_bfe_u32 v110, v101, 16, 4
	v_lshl_add_u32 v110, v110, 3, s66
	ds_read_b64 v[58:59], v110
	v_bfe_u32 v111, v101, 24, 4
	v_lshl_add_u32 v111, v111, 3, s66
	ds_read_b64 v[60:61], v111
	v_xor_b32_e32 v110, 16, v38
	v_xor_b32_e32 v111, 32, v38
	v_xor_b32_e32 v39, 48, v38
	s_waitcnt lgkmcnt(0)
	ds_read_b128 v[86:89], v38
	ds_read_b128 v[90:93], v110
	ds_read_b128 v[94:97], v111
	ds_read_b128 v[102:105], v39
	ds_read_b128 v[62:65], v99
	ds_read_b128 v[42:45], v99 offset:1024
	s_waitcnt lgkmcnt(1)
	v_mfma_f32_32x32x16_f16 v[112:127], v[86:89], v[62:65], 0
	ds_read_b128 v[62:65], v99 offset:2048
	s_waitcnt lgkmcnt(1)
	v_mfma_f32_32x32x16_f16 v[112:127], v[90:93], v[42:45], v[112:127]
	ds_read_b128 v[42:45], v99 offset:3072
	s_waitcnt lgkmcnt(1)
	v_mfma_f32_32x32x16_f16 v[112:127], v[94:97], v[62:65], v[112:127]
	ds_read_b128 v[62:65], v99 offset:4096
	s_waitcnt lgkmcnt(1)
	v_mfma_f32_32x32x16_f16 v[112:127], v[102:105], v[42:45], v[112:127]
	ds_read_b128 v[42:45], v99 offset:5120
	s_nop 11
	v_fma_f32 v110, v66, v112, v68
	v_fma_f32 v111, v66, v113, v68
	v_max_f32_e32 v110, 0, v110
	v_max_f32_e32 v111, 0, v111
	v_cvt_pk_bf16_f32 v106, v110, v111
	v_fma_f32 v110, v66, v114, v68
	v_fma_f32 v111, v66, v115, v68
	v_max_f32_e32 v110, 0, v110
	v_max_f32_e32 v111, 0, v111
	v_cvt_pk_bf16_f32 v107, v110, v111
	v_fma_f32 v110, v66, v116, v68
	v_fma_f32 v111, v66, v117, v68
	v_max_f32_e32 v110, 0, v110
	v_max_f32_e32 v111, 0, v111
	v_cvt_pk_bf16_f32 v108, v110, v111
	v_fma_f32 v110, v66, v118, v68
	v_fma_f32 v111, v66, v119, v68
	v_max_f32_e32 v110, 0, v110
	v_max_f32_e32 v111, 0, v111
	v_cvt_pk_bf16_f32 v109, v110, v111
	s_nop 1
	v_mfma_f32_32x32x16_bf16 v[18:33], v[106:109], v[54:57], v[18:33]
	v_fma_f32 v110, v66, v120, v68
	v_fma_f32 v111, v66, v121, v68
	v_max_f32_e32 v110, 0, v110
	v_max_f32_e32 v111, 0, v111
	v_cvt_pk_bf16_f32 v106, v110, v111
	v_fma_f32 v110, v66, v122, v68
	v_fma_f32 v111, v66, v123, v68
	v_max_f32_e32 v110, 0, v110
	v_max_f32_e32 v111, 0, v111
	v_cvt_pk_bf16_f32 v107, v110, v111
	v_fma_f32 v110, v66, v124, v68
	v_fma_f32 v111, v66, v125, v68
	v_max_f32_e32 v110, 0, v110
	v_max_f32_e32 v111, 0, v111
	v_cvt_pk_bf16_f32 v108, v110, v111
	v_fma_f32 v110, v66, v126, v68
	v_fma_f32 v111, v66, v127, v68
	v_max_f32_e32 v110, 0, v110
	v_max_f32_e32 v111, 0, v111
	v_cvt_pk_bf16_f32 v109, v110, v111
	s_nop 1
	v_mfma_f32_32x32x16_bf16 v[18:33], v[106:109], v[58:61], v[18:33]
	s_waitcnt lgkmcnt(1)
	v_mfma_f32_32x32x16_f16 v[112:127], v[86:89], v[62:65], 0
	ds_read_b128 v[62:65], v99 offset:6144
	s_waitcnt lgkmcnt(1)
	v_mfma_f32_32x32x16_f16 v[112:127], v[90:93], v[42:45], v[112:127]
	ds_read_b128 v[42:45], v99 offset:7168
	s_waitcnt lgkmcnt(1)
	v_mfma_f32_32x32x16_f16 v[112:127], v[94:97], v[62:65], v[112:127]
	s_waitcnt lgkmcnt(0)
	v_mfma_f32_32x32x16_f16 v[112:127], v[102:105], v[42:45], v[112:127]
	s_cmp_eq_u32 s15, 1
	s_cbranch_scc1 .Lcu_skip2
	global_load_dwordx4 v[86:89], v46, s[10:11]
	global_load_dwordx4 v[90:93], v47, s[10:11]
	global_load_dwordx4 v[94:97], v48, s[10:11]
	global_load_dwordx4 v[102:105], v49, s[10:11]
	s_add_i32 s34, s34, 0x80
	v_add_u32_e32 v39, s34, v35
	global_load_dwordx4 v[42:45], v39, s[4:5]
	global_load_dwordx4 v[46:49], v39, s[6:7]

	.amdhsa_kernel _Z8k_passCUILi1EEvPKiS1_PKfPKtS5_S3_S3_S3_S3_S3_S3_PK15HIP_vector_typeIjLj4EES9_S9_PKdSB_S1_S1_S5_S3_PtPd
		.amdhsa_group_segment_fixed_size 79232
		.amdhsa_private_segment_fixed_size 0
		.amdhsa_kernarg_size 432
		.amdhsa_user_sgpr_count 2
		.amdhsa_user_sgpr_dispatch_ptr 0
		.amdhsa_user_sgpr_queue_ptr 0
		.amdhsa_user_sgpr_kernarg_segment_ptr 1
		.amdhsa_user_sgpr_dispatch_id 0
		.amdhsa_user_sgpr_kernarg_preload_length 0
		.amdhsa_user_sgpr_kernarg_preload_offset 0
		.amdhsa_user_sgpr_private_segment_size 0
		.amdhsa_uses_dynamic_stack 0
		.amdhsa_enable_private_segment 0
		.amdhsa_system_sgpr_workgroup_id_x 1
		.amdhsa_system_sgpr_workgroup_id_y 0
		.amdhsa_system_sgpr_workgroup_id_z 0
		.amdhsa_system_sgpr_workgroup_info 0
		.amdhsa_system_vgpr_workitem_id 0
		.amdhsa_next_free_vgpr 128
		.amdhsa_next_free_sgpr 91
		.amdhsa_accum_offset 128
		.amdhsa_reserve_vcc 1
		.amdhsa_float_round_mode_32 0
		.amdhsa_float_round_mode_16_64 0
		.amdhsa_float_denorm_mode_32 3
		.amdhsa_float_denorm_mode_16_64 3
		.amdhsa_dx10_clamp 1
		.amdhsa_ieee_mode 1
		.amdhsa_fp16_overflow 0
		.amdhsa_tg_split 0
		.amdhsa_exception_fp_ieee_invalid_op 0
		.amdhsa_exception_fp_denorm_src 0
		.amdhsa_exception_fp_ieee_div_zero 0
		.amdhsa_exception_fp_ieee_overflow 0
		.amdhsa_exception_fp_ieee_underflow 0
		.amdhsa_exception_fp_ieee_inexact 0
		.amdhsa_exception_int_div_zero 0
	.end_amdhsa_kernel

amdhsa.kernels:
  - .agpr_count:     0
    .args:
      - .actual_access:  read_only
        .address_space:  global
        .offset:         0
        .size:           8
        .value_kind:     global_buffer
      - .actual_access:  read_only
        .address_space:  global
        .offset:         8
        .size:           8
        .value_kind:     global_buffer
      - .actual_access:  read_only
        .address_space:  global
        .offset:         16
        .size:           8
        .value_kind:     global_buffer
      - .actual_access:  read_only
        .address_space:  global
        .offset:         24
        .size:           8
        .value_kind:     global_buffer
      - .actual_access:  write_only
        .address_space:  global
        .offset:         32
        .size:           8
        .value_kind:     global_buffer
      - .actual_access:  write_only
        .address_space:  global
        .offset:         40
        .size:           8
        .value_kind:     global_buffer
      - .actual_access:  write_only
        .address_space:  global
        .offset:         48
        .size:           8
        .value_kind:     global_buffer
      - .offset:         56
        .size:           4
        .value_kind:     hidden_block_count_x
      - .offset:         60
        .size:           4
        .value_kind:     hidden_block_count_y
      - .offset:         64
        .size:           4
        .value_kind:     hidden_block_count_z
      - .offset:         68
        .size:           2
        .value_kind:     hidden_group_size_x
      - .offset:         70
        .size:           2
        .value_kind:     hidden_group_size_y
      - .offset:         72
        .size:           2
        .value_kind:     hidden_group_size_z
      - .offset:         74
        .size:           2
        .value_kind:     hidden_remainder_x
      - .offset:         76
        .size:           2
        .value_kind:     hidden_remainder_y
      - .offset:         78
        .size:           2
        .value_kind:     hidden_remainder_z
      - .offset:         96
        .size:           8
        .value_kind:     hidden_global_offset_x
      - .offset:         104
        .size:           8
        .value_kind:     hidden_global_offset_y
      - .offset:         112
        .size:           8
        .value_kind:     hidden_global_offset_z
      - .offset:         120
        .size:           2
        .value_kind:     hidden_grid_dims
    .group_segment_fixed_size: 0
    .kernarg_segment_align: 8
    .kernarg_segment_size: 312
    .language:       OpenCL C
    .language_version:
      - 2
      - 0
    .max_flat_workgroup_size: 256
    .name:           _Z6k_prepPKfS0_S0_S0_P15HIP_vector_typeIjLj4EEPiPd
    .private_segment_fixed_size: 0
    .sgpr_count:     25
    .sgpr_spill_count: 0
    .symbol:         _Z6k_prepPKfS0_S0_S0_P15HIP_vector_typeIjLj4EEPiPd.kd
    .uniform_work_group_size: 1
    .uses_dynamic_stack: false
    .vgpr_count:     24
    .vgpr_spill_count: 0
    .wavefront_size: 64
  - .agpr_count:     0
    .args:
      - .actual_access:  read_only
        .address_space:  global
        .offset:         0
        .size:           8
        .value_kind:     global_buffer
      - .actual_access:  read_only
        .address_space:  global
        .offset:         8
        .size:           8
        .value_kind:     global_buffer
      - .actual_access:  read_only
        .address_space:  global
        .offset:         16
        .size:           8
        .value_kind:     global_buffer
      - .actual_access:  read_only
        .address_space:  global
        .offset:         24
        .size:           8
        .value_kind:     global_buffer
      - .actual_access:  read_only
        .address_space:  global
        .offset:         32
        .size:           8
        .value_kind:     global_buffer
      - .actual_access:  write_only
        .address_space:  global
        .offset:         40
        .size:           8
        .value_kind:     global_buffer
      - .actual_access:  write_only
        .address_space:  global
        .offset:         48
        .size:           8
        .value_kind:     global_buffer
    .group_segment_fixed_size: 4112
    .kernarg_segment_align: 8
    .kernarg_segment_size: 56
    .language:       OpenCL C
    .language_version:
      - 2
      - 0
    .max_flat_workgroup_size: 256
    .name:           _Z10k_bscatterPKiS0_PKfS0_S0_PiP15HIP_vector_typeIjLj2EE
    .private_segment_fixed_size: 0
    .sgpr_count:     28
    .sgpr_spill_count: 0
    .symbol:         _Z10k_bscatterPKiS0_PKfS0_S0_PiP15HIP_vector_typeIjLj2EE.kd
    .uniform_work_group_size: 1
    .uses_dynamic_stack: false
    .vgpr_count:     78
    .vgpr_spill_count: 0
    .wavefront_size: 64
  - .agpr_count:     0
    .args:
      - .actual_access:  read_only
        .address_space:  global
        .offset:         0
        .size:           8
        .value_kind:     global_buffer
      - .actual_access:  read_only
        .address_space:  global
        .offset:         8
        .size:           8
        .value_kind:     global_buffer
      - .actual_access:  write_only
        .address_space:  global
        .offset:         16
        .size:           8
        .value_kind:     global_buffer
      - .actual_access:  write_only
        .address_space:  global
        .offset:         24
        .size:           8
        .value_kind:     global_buffer
      - .actual_access:  write_only
        .address_space:  global
        .offset:         32
        .size:           8
        .value_kind:     global_buffer
      - .actual_access:  write_only
        .address_space:  global
        .offset:         40
        .size:           8
        .value_kind:     global_buffer
    .group_segment_fixed_size: 29200
    .kernarg_segment_align: 8
    .kernarg_segment_size: 48
    .language:       OpenCL C
    .language_version:
      - 2
      - 0
    .max_flat_workgroup_size: 256
    .name:           _Z7k_bsortPKiPK15HIP_vector_typeIjLj2EEPiS5_S5_Pf
    .private_segment_fixed_size: 0
    .sgpr_count:     106
    .sgpr_spill_count: 12
    .symbol:         _Z7k_bsortPKiPK15HIP_vector_typeIjLj2EEPiS5_S5_Pf.kd
    .uniform_work_group_size: 1
    .uses_dynamic_stack: false
    .vgpr_count:     69
    .vgpr_spill_count: 0
    .wavefront_size: 64
  - .agpr_count:     32
    .args:
      - .address_space:  global
        .offset:         0
        .size:           8
        .value_kind:     global_buffer
      - .actual_access:  read_only
        .address_space:  global
        .offset:         8
        .size:           8
        .value_kind:     global_buffer
      - .actual_access:  read_only
        .address_space:  global
        .offset:         16
        .size:           8
        .value_kind:     global_buffer
      - .actual_access:  read_only
        .address_space:  global
        .offset:         24
        .size:           8
        .value_kind:     global_buffer
      - .actual_access:  read_only
        .address_space:  global
        .offset:         32
        .size:           8
        .value_kind:     global_buffer
      - .actual_access:  read_only
        .address_space:  global
        .offset:         40
        .size:           8
        .value_kind:     global_buffer
      - .address_space:  global
        .offset:         48
        .size:           8
        .value_kind:     global_buffer
      - .address_space:  global
        .offset:         56
        .size:           8
        .value_kind:     global_buffer
      - .offset:         64
        .size:           4
        .value_kind:     hidden_block_count_x
      - .offset:         68
        .size:           4
        .value_kind:     hidden_block_count_y
      - .offset:         72
        .size:           4
        .value_kind:     hidden_block_count_z
      - .offset:         76
        .size:           2
        .value_kind:     hidden_group_size_x
      - .offset:         78
        .size:           2
        .value_kind:     hidden_group_size_y
      - .offset:         80
        .size:           2
        .value_kind:     hidden_group_size_z
      - .offset:         82
        .size:           2
        .value_kind:     hidden_remainder_x
      - .offset:         84
        .size:           2
        .value_kind:     hidden_remainder_y
      - .offset:         86
        .size:           2
        .value_kind:     hidden_remainder_z
      - .offset:         104
        .size:           8
        .value_kind:     hidden_global_offset_x
      - .offset:         112
        .size:           8
        .value_kind:     hidden_global_offset_y
      - .offset:         120
        .size:           8
        .value_kind:     hidden_global_offset_z
      - .offset:         128
        .size:           2
        .value_kind:     hidden_grid_dims
    .group_segment_fixed_size: 18944
    .kernarg_segment_align: 8
    .kernarg_segment_size: 320
    .language:       OpenCL C
    .language_version:
      - 2
      - 0
    .max_flat_workgroup_size: 256
    .name:           _Z4k_U2PKtPK15HIP_vector_typeIjLj4EEPKdPKfS8_S8_PtPd
    .private_segment_fixed_size: 0
    .sgpr_count:     34
    .sgpr_spill_count: 0
    .symbol:         _Z4k_U2PKtPK15HIP_vector_typeIjLj4EEPKdPKfS8_S8_PtPd.kd
    .uniform_work_group_size: 1
    .uses_dynamic_stack: false
    .vgpr_count:     104
    .vgpr_spill_count: 0
    .wavefront_size: 64
  - .agpr_count:     0
    .args:
      - .actual_access:  read_only
        .address_space:  global
        .offset:         0
        .size:           8
        .value_kind:     global_buffer
      - .actual_access:  read_only
        .address_space:  global
        .offset:         8
        .size:           8
        .value_kind:     global_buffer
      - .actual_access:  write_only
        .address_space:  global
        .offset:         16
        .size:           8
        .value_kind:     global_buffer
    .group_segment_fixed_size: 0
    .kernarg_segment_align: 8
    .kernarg_segment_size: 24
    .language:       OpenCL C
    .language_version:
      - 2
      - 0
    .max_flat_workgroup_size: 1024
    .name:           _Z7k_finalPKdPKfPf
    .private_segment_fixed_size: 0
    .sgpr_count:     28
    .sgpr_spill_count: 0
    .symbol:         _Z7k_finalPKdPKfPf.kd
    .uniform_work_group_size: 1
    .uses_dynamic_stack: false
    .vgpr_count:     10
    .vgpr_spill_count: 0
    .wavefront_size: 64
  - .agpr_count:     64
    .args:
      - .actual_access:  read_only
        .address_space:  global
        .offset:         0
        .size:           8
        .value_kind:     global_buffer
      - .address_space:  global
        .offset:         8
        .size:           8
        .value_kind:     global_buffer
      - .actual_access:  write_only
        .address_space:  global
        .offset:         16
        .size:           8
        .value_kind:     global_buffer
      - .actual_access:  read_only
        .address_space:  global
        .offset:         24
        .size:           8
        .value_kind:     global_buffer
      - .actual_access:  read_only
        .address_space:  global
        .offset:         32
        .size:           8
        .value_kind:     global_buffer
      - .actual_access:  read_only
        .address_space:  global
        .offset:         40
        .size:           8
        .value_kind:     global_buffer
      - .actual_access:  read_only
        .address_space:  global
        .offset:         48
        .size:           8
        .value_kind:     global_buffer
      - .actual_access:  read_only
        .address_space:  global
        .offset:         56
        .size:           8
        .value_kind:     global_buffer
      - .actual_access:  write_only
        .address_space:  global
        .offset:         64
        .size:           8
        .value_kind:     global_buffer
      - .actual_access:  write_only
        .address_space:  global
        .offset:         72
        .size:           8
        .value_kind:     global_buffer
      - .actual_access:  write_only
        .address_space:  global
        .offset:         80
        .size:           8
        .value_kind:     global_buffer
      - .offset:         88
        .size:           4
        .value_kind:     hidden_block_count_x
      - .offset:         92
        .size:           4
        .value_kind:     hidden_block_count_y
      - .offset:         96
        .size:           4
        .value_kind:     hidden_block_count_z
      - .offset:         100
        .size:           2
        .value_kind:     hidden_group_size_x
      - .offset:         102
        .size:           2
        .value_kind:     hidden_group_size_y
      - .offset:         104
        .size:           2
        .value_kind:     hidden_group_size_z
      - .offset:         106
        .size:           2
        .value_kind:     hidden_remainder_x
      - .offset:         108
        .size:           2
        .value_kind:     hidden_remainder_y
      - .offset:         110
        .size:           2
        .value_kind:     hidden_remainder_z
      - .offset:         128
        .size:           8
        .value_kind:     hidden_global_offset_x
      - .offset:         136
        .size:           8
        .value_kind:     hidden_global_offset_y
      - .offset:         144
        .size:           8
        .value_kind:     hidden_global_offset_z
      - .offset:         152
        .size:           2
        .value_kind:     hidden_grid_dims
    .group_segment_fixed_size: 45312
    .kernarg_segment_align: 8
    .kernarg_segment_size: 344
    .language:       OpenCL C
    .language_version:
      - 2
      - 0
    .max_flat_workgroup_size: 256
    .name:           _Z14k_bcount_node0ItEvPKiPiS2_PKfS4_S4_S4_PK15HIP_vector_typeIjLj4EEPtPT_SB_
    .private_segment_fixed_size: 0
    .sgpr_count:     26
    .sgpr_spill_count: 0
    .symbol:         _Z14k_bcount_node0ItEvPKiPiS2_PKfS4_S4_S4_PK15HIP_vector_typeIjLj4EEPtPT_SB_.kd
    .uniform_work_group_size: 1
    .uses_dynamic_stack: false
    .vgpr_count:     104
    .vgpr_spill_count: 0
    .wavefront_size: 64
  - .agpr_count:     0
    .args:
      - .actual_access:  read_only
        .address_space:  global
        .offset:         0
        .size:           8
        .value_kind:     global_buffer
      - .actual_access:  read_only
        .address_space:  global
        .offset:         8
        .size:           8
        .value_kind:     global_buffer
      - .actual_access:  read_only
        .address_space:  global
        .offset:         16
        .size:           8
        .value_kind:     global_buffer
      - .actual_access:  read_only
        .address_space:  global
        .offset:         24
        .size:           8
        .value_kind:     global_buffer
      - .actual_access:  read_only
        .address_space:  global
        .offset:         32
        .size:           8
        .value_kind:     global_buffer
      - .actual_access:  read_only
        .address_space:  global
        .offset:         40
        .size:           8
        .value_kind:     global_buffer
      - .address_space:  global
        .offset:         48
        .size:           8
        .value_kind:     global_buffer
      - .offset:         56
        .size:           4
        .value_kind:     hidden_block_count_x
      - .offset:         60
        .size:           4
        .value_kind:     hidden_block_count_y
      - .offset:         64
        .size:           4
        .value_kind:     hidden_block_count_z
      - .offset:         68
        .size:           2
        .value_kind:     hidden_group_size_x
      - .offset:         70
        .size:           2
        .value_kind:     hidden_group_size_y
      - .offset:         72
        .size:           2
        .value_kind:     hidden_group_size_z
      - .offset:         74
        .size:           2
        .value_kind:     hidden_remainder_x
      - .offset:         76
        .size:           2
        .value_kind:     hidden_remainder_y
      - .offset:         78
        .size:           2
        .value_kind:     hidden_remainder_z
      - .offset:         96
        .size:           8
        .value_kind:     hidden_global_offset_x
      - .offset:         104
        .size:           8
        .value_kind:     hidden_global_offset_y
      - .offset:         112
        .size:           8
        .value_kind:     hidden_global_offset_z
      - .offset:         120
        .size:           2
        .value_kind:     hidden_grid_dims
    .group_segment_fixed_size: 2048
    .kernarg_segment_align: 8
    .kernarg_segment_size: 312
    .language:       OpenCL C
    .language_version:
      - 2
      - 0
    .max_flat_workgroup_size: 256
    .name:           _Z7k_passAItEvPKiS1_PKfPKT_S6_S3_Pd
    .private_segment_fixed_size: 0
    .sgpr_count:     36
    .sgpr_spill_count: 0
    .symbol:         _Z7k_passAItEvPKiS1_PKfPKT_S6_S3_Pd.kd
    .uniform_work_group_size: 1
    .uses_dynamic_stack: false
    .vgpr_count:     104
    .vgpr_spill_count: 0
    .wavefront_size: 64
  - .agpr_count:     0
    .args:
      - .actual_access:  read_only
        .address_space:  global
        .offset:         0
        .size:           8
        .value_kind:     global_buffer
      - .actual_access:  read_only
        .address_space:  global
        .offset:         8
        .size:           8
        .value_kind:     global_buffer
      - .actual_access:  read_only
        .address_space:  global
        .offset:         16
        .size:           8
        .value_kind:     global_buffer
      - .actual_access:  read_only
        .address_space:  global
        .offset:         24
        .size:           8
        .value_kind:     global_buffer
      - .actual_access:  read_only
        .address_space:  global
        .offset:         32
        .size:           8
        .value_kind:     global_buffer
      - .actual_access:  read_only
        .address_space:  global
        .offset:         40
        .size:           8
        .value_kind:     global_buffer
      - .actual_access:  read_only
        .address_space:  global
        .offset:         48
        .size:           8
        .value_kind:     global_buffer
      - .actual_access:  read_only
        .address_space:  global
        .offset:         56
        .size:           8
        .value_kind:     global_buffer
      - .actual_access:  read_only
        .address_space:  global
        .offset:         64
        .size:           8
        .value_kind:     global_buffer
      - .actual_access:  read_only
        .address_space:  global
        .offset:         72
        .size:           8
        .value_kind:     global_buffer
      - .actual_access:  read_only
        .address_space:  global
        .offset:         80
        .size:           8
        .value_kind:     global_buffer
      - .actual_access:  read_only
        .address_space:  global
        .offset:         88
        .size:           8
        .value_kind:     global_buffer
      - .actual_access:  read_only
        .address_space:  global
        .offset:         96
        .size:           8
        .value_kind:     global_buffer
      - .address_space:  global
        .offset:         104
        .size:           8
        .value_kind:     global_buffer
      - .actual_access:  read_only
        .address_space:  global
        .offset:         112
        .size:           8
        .value_kind:     global_buffer
      - .actual_access:  read_only
        .address_space:  global
        .offset:         120
        .size:           8
        .value_kind:     global_buffer
      - .address_space:  global
        .offset:         128
        .size:           8
        .value_kind:     global_buffer
      - .offset:         136
        .size:           4
        .value_kind:     hidden_block_count_x
      - .offset:         140
        .size:           4
        .value_kind:     hidden_block_count_y
      - .offset:         144
        .size:           4
        .value_kind:     hidden_block_count_z
      - .offset:         148
        .size:           2
        .value_kind:     hidden_group_size_x
      - .offset:         150
        .size:           2
        .value_kind:     hidden_group_size_y
      - .offset:         152
        .size:           2
        .value_kind:     hidden_group_size_z
      - .offset:         154
        .size:           2
        .value_kind:     hidden_remainder_x
      - .offset:         156
        .size:           2
        .value_kind:     hidden_remainder_y
      - .offset:         158
        .size:           2
        .value_kind:     hidden_remainder_z
      - .offset:         176
        .size:           8
        .value_kind:     hidden_global_offset_x
      - .offset:         184
        .size:           8
        .value_kind:     hidden_global_offset_y
      - .offset:         192
        .size:           8
        .value_kind:     hidden_global_offset_z
      - .offset:         200
        .size:           2
        .value_kind:     hidden_grid_dims
    .group_segment_fixed_size: 37632
    .kernarg_segment_align: 8
    .kernarg_segment_size: 392
    .language:       OpenCL C
    .language_version:
      - 2
      - 0
    .max_flat_workgroup_size: 256
    .name:           _Z7k_passLILi1ELi0ELi1EEvPKiS1_PKfPKtS5_S3_S3_S3_S3_S3_S3_PK15HIP_vector_typeIjLj4EEPKdPdS1_PtS1_
    .private_segment_fixed_size: 0
    .sgpr_count:     62
    .sgpr_spill_count: 0
    .symbol:         _Z7k_passLILi1ELi0ELi1EEvPKiS1_PKfPKtS5_S3_S3_S3_S3_S3_S3_PK15HIP_vector_typeIjLj4EEPKdPdS1_PtS1_.kd
    .uniform_work_group_size: 1
    .uses_dynamic_stack: false
    .vgpr_count:     128
    .vgpr_spill_count: 0
    .wavefront_size: 64
  - .agpr_count:     0
    .args:
      - .actual_access:  read_only
        .address_space:  global
        .offset:         0
        .size:           8
        .value_kind:     global_buffer
      - .actual_access:  read_only
        .address_space:  global
        .offset:         8
        .size:           8
        .value_kind:     global_buffer
      - .actual_access:  read_only
        .address_space:  global
        .offset:         16
        .size:           8
        .value_kind:     global_buffer
      - .actual_access:  read_only
        .address_space:  global
        .offset:         24
        .size:           8
        .value_kind:     global_buffer
      - .actual_access:  read_only
        .address_space:  global
        .offset:         32
        .size:           8
        .value_kind:     global_buffer
      - .actual_access:  read_only
        .address_space:  global
        .offset:         40
        .size:           8
        .value_kind:     global_buffer
      - .actual_access:  read_only
        .address_space:  global
        .offset:         48
        .size:           8
        .value_kind:     global_buffer
      - .actual_access:  read_only
        .address_space:  global
        .offset:         56
        .size:           8
        .value_kind:     global_buffer
      - .actual_access:  read_only
        .address_space:  global
        .offset:         64
        .size:           8
        .value_kind:     global_buffer
      - .actual_access:  read_only
        .address_space:  global
        .offset:         72
        .size:           8
        .value_kind:     global_buffer
      - .actual_access:  read_only
        .address_space:  global
        .offset:         80
        .size:           8
        .value_kind:     global_buffer
      - .actual_access:  read_only
        .address_space:  global
        .offset:         88
        .size:           8
        .value_kind:     global_buffer
      - .actual_access:  read_only
        .address_space:  global
        .offset:         96
        .size:           8
        .value_kind:     global_buffer
      - .actual_access:  read_only
        .address_space:  global
        .offset:         104
        .size:           8
        .value_kind:     global_buffer
      - .actual_access:  read_only
        .address_space:  global
        .offset:         112
        .size:           8
        .value_kind:     global_buffer
      - .actual_access:  read_only
        .address_space:  global
        .offset:         120
        .size:           8
        .value_kind:     global_buffer
      - .actual_access:  read_only
        .address_space:  global
        .offset:         128
        .size:           8
        .value_kind:     global_buffer
      - .address_space:  global
        .offset:         136
        .size:           8
        .value_kind:     global_buffer
      - .actual_access:  read_only
        .address_space:  global
        .offset:         144
        .size:           8
        .value_kind:     global_buffer
      - .actual_access:  read_only
        .address_space:  global
        .offset:         152
        .size:           8
        .value_kind:     global_buffer
      - .actual_access:  write_only
        .address_space:  global
        .offset:         160
        .size:           8
        .value_kind:     global_buffer
      - .address_space:  global
        .offset:         168
        .size:           8
        .value_kind:     global_buffer
      - .offset:         176
        .size:           4
        .value_kind:     hidden_block_count_x
      - .offset:         180
        .size:           4
        .value_kind:     hidden_block_count_y
      - .offset:         184
        .size:           4
        .value_kind:     hidden_block_count_z
      - .offset:         188
        .size:           2
        .value_kind:     hidden_group_size_x
      - .offset:         190
        .size:           2
        .value_kind:     hidden_group_size_y
      - .offset:         192
        .size:           2
        .value_kind:     hidden_group_size_z
      - .offset:         194
        .size:           2
        .value_kind:     hidden_remainder_x
      - .offset:         196
        .size:           2
        .value_kind:     hidden_remainder_y
      - .offset:         198
        .size:           2
        .value_kind:     hidden_remainder_z
      - .offset:         216
        .size:           8
        .value_kind:     hidden_global_offset_x
      - .offset:         224
        .size:           8
        .value_kind:     hidden_global_offset_y
      - .offset:         232
        .size:           8
        .value_kind:     hidden_global_offset_z
      - .offset:         240
        .size:           2
        .value_kind:     hidden_grid_dims
    .group_segment_fixed_size: 79232
    .kernarg_segment_align: 8
    .kernarg_segment_size: 432
    .language:       OpenCL C
    .language_version:
      - 2
      - 0
    .max_flat_workgroup_size: 512
    .name:           _Z8k_passCUILi1EEvPKiS1_PKfPKtS5_S3_S3_S3_S3_S3_S3_PK15HIP_vector_typeIjLj4EES9_S9_PKdSB_S1_S1_S5_S3_PtPd
    .private_segment_fixed_size: 0
    .sgpr_count:     35
    .sgpr_spill_count: 0
    .symbol:         _Z8k_passCUILi1EEvPKiS1_PKfPKtS5_S3_S3_S3_S3_S3_S3_PK15HIP_vector_typeIjLj4EES9_S9_PKdSB_S1_S1_S5_S3_PtPd.kd
    .uniform_work_group_size: 1
    .uses_dynamic_stack: false
    .vgpr_count:     128
    .vgpr_spill_count: 0
    .wavefront_size: 64
  - .agpr_count:     64
    .args:
      - .actual_access:  read_only
        .address_space:  global
        .offset:         0
        .size:           8
        .value_kind:     global_buffer
      - .address_space:  global
        .offset:         8
        .size:           8
        .value_kind:     global_buffer
      - .actual_access:  read_only
        .address_space:  global
        .offset:         16
        .size:           8
        .value_kind:     global_buffer
      - .actual_access:  read_only
        .address_space:  global
        .offset:         24
        .size:           8
        .value_kind:     global_buffer
      - .actual_access:  read_only
        .address_space:  global
        .offset:         32
        .size:           8
        .value_kind:     global_buffer
      - .actual_access:  read_only
        .address_space:  global
        .offset:         40
        .size:           8
        .value_kind:     global_buffer
      - .actual_access:  read_only
        .address_space:  global
        .offset:         48
        .size:           8
        .value_kind:     global_buffer
      - .actual_access:  write_only
        .address_space:  global
        .offset:         56
        .size:           8
        .value_kind:     global_buffer
      - .actual_access:  write_only
        .address_space:  global
        .offset:         64
        .size:           8
        .value_kind:     global_buffer
      - .actual_access:  read_only
        .address_space:  global
        .offset:         72
        .size:           8
        .value_kind:     global_buffer
      - .actual_access:  read_only
        .address_space:  global
        .offset:         80
        .size:           8
        .value_kind:     global_buffer
      - .offset:         88
        .size:           4
        .value_kind:     hidden_block_count_x
      - .offset:         92
        .size:           4
        .value_kind:     hidden_block_count_y
      - .offset:         96
        .size:           4
        .value_kind:     hidden_block_count_z
      - .offset:         100
        .size:           2
        .value_kind:     hidden_group_size_x
      - .offset:         102
        .size:           2
        .value_kind:     hidden_group_size_y
      - .offset:         104
        .size:           2
        .value_kind:     hidden_group_size_z
      - .offset:         106
        .size:           2
        .value_kind:     hidden_remainder_x
      - .offset:         108
        .size:           2
        .value_kind:     hidden_remainder_y
      - .offset:         110
        .size:           2
        .value_kind:     hidden_remainder_z
      - .offset:         128
        .size:           8
        .value_kind:     hidden_global_offset_x
      - .offset:         136
        .size:           8
        .value_kind:     hidden_global_offset_y
      - .offset:         144
        .size:           8
        .value_kind:     hidden_global_offset_z
      - .offset:         152
        .size:           2
        .value_kind:     hidden_grid_dims
    .group_segment_fixed_size: 33280
    .kernarg_segment_align: 8
    .kernarg_segment_size: 344
    .language:       OpenCL C
    .language_version:
      - 2
      - 0
    .max_flat_workgroup_size: 256
    .name:           _Z4k_U3ILb0EtEvPKtPtPKdPKfS6_PK15HIP_vector_typeIjLj4EES6_PT0_SC_S6_Pd
    .private_segment_fixed_size: 0
    .sgpr_count:     20
    .sgpr_spill_count: 0
    .symbol:         _Z4k_U3ILb0EtEvPKtPtPKdPKfS6_PK15HIP_vector_typeIjLj4EES6_PT0_SC_S6_Pd.kd
    .uniform_work_group_size: 1
    .uses_dynamic_stack: false
    .vgpr_count:     144
    .vgpr_spill_count: 0
    .wavefront_size: 64
  - .agpr_count:     0
    .args:
      - .actual_access:  read_only
        .address_space:  global
        .offset:         0
        .size:           8
        .value_kind:     global_buffer
      - .actual_access:  read_only
        .address_space:  global
        .offset:         8
        .size:           8
        .value_kind:     global_buffer
      - .actual_access:  read_only
        .address_space:  global
        .offset:         16
        .size:           8
        .value_kind:     global_buffer
      - .actual_access:  read_only
        .address_space:  global
        .offset:         24
        .size:           8
        .value_kind:     global_buffer
      - .actual_access:  read_only
        .address_space:  global
        .offset:         32
        .size:           8
        .value_kind:     global_buffer
      - .actual_access:  read_only
        .address_space:  global
        .offset:         40
        .size:           8
        .value_kind:     global_buffer
      - .actual_access:  read_only
        .address_space:  global
        .offset:         48
        .size:           8
        .value_kind:     global_buffer
      - .actual_access:  read_only
        .address_space:  global
        .offset:         56
        .size:           8
        .value_kind:     global_buffer
      - .actual_access:  read_only
        .address_space:  global
        .offset:         64
        .size:           8
        .value_kind:     global_buffer
      - .actual_access:  read_only
        .address_space:  global
        .offset:         72
        .size:           8
        .value_kind:     global_buffer
      - .address_space:  global
        .offset:         80
        .size:           8
        .value_kind:     global_buffer
      - .offset:         88
        .size:           4
        .value_kind:     hidden_block_count_x
      - .offset:         92
        .size:           4
        .value_kind:     hidden_block_count_y
      - .offset:         96
        .size:           4
        .value_kind:     hidden_block_count_z
      - .offset:         100
        .size:           2
        .value_kind:     hidden_group_size_x
      - .offset:         102
        .size:           2
        .value_kind:     hidden_group_size_y
      - .offset:         104
        .size:           2
        .value_kind:     hidden_group_size_z
      - .offset:         106
        .size:           2
        .value_kind:     hidden_remainder_x
      - .offset:         108
        .size:           2
        .value_kind:     hidden_remainder_y
      - .offset:         110
        .size:           2
        .value_kind:     hidden_remainder_z
      - .offset:         128
        .size:           8
        .value_kind:     hidden_global_offset_x
      - .offset:         136
        .size:           8
        .value_kind:     hidden_global_offset_y
      - .offset:         144
        .size:           8
        .value_kind:     hidden_global_offset_z
      - .offset:         152
        .size:           2
        .value_kind:     hidden_grid_dims
    .group_segment_fixed_size: 784
    .kernarg_segment_align: 8
    .kernarg_segment_size: 344
    .language:       OpenCL C
    .language_version:
      - 2
      - 0
    .max_flat_workgroup_size: 256
    .name:           _Z4k_U3ILb1EtEvPKtPtPKdPKfS6_PK15HIP_vector_typeIjLj4EES6_PT0_SC_S6_Pd
    .private_segment_fixed_size: 0
    .sgpr_count:     20
    .sgpr_spill_count: 0
    .symbol:         _Z4k_U3ILb1EtEvPKtPtPKdPKfS6_PK15HIP_vector_typeIjLj4EES6_PT0_SC_S6_Pd.kd
    .uniform_work_group_size: 1
    .uses_dynamic_stack: false
    .vgpr_count:     79
    .vgpr_spill_count: 0
    .wavefront_size: 64
